# P2 SWA: first query sub-block q/rope loads also issued at unit start (K staging on separate registers)
# speedup vs baseline: 1.0824x; 1.0009x over previous
; #define LAS __attribute__((address_space(3)))
; __device__ __forceinline__ void swa_unit(Frame& F, int b, int kvh, int qb) {
;     ...
;     for (int task = tid; task < 1536; task += NTHREADS) { const int key = task >> 3, c = task & 7, kg = K0 + key;
;         u32x4 v = (u32x4){0u, 0u, 0u, 0u};
;         if (kg >= 0) v = *(const u32x4*)(PROJ + (rowb + kg) * LDP + C_SV + kvh * 64 + 8 * c);
;         *(LAS u32x4*)(Vl + key * SWA_KROW + 16 * c) = v; }
;     __syncthreads();
;     const int qh = kvh * 8 + F.wave;
;     const float sink2 = F.sinks[qh] * 1.4426950408889634f;
; #pragma unroll 1
;     for (int sub = 0; sub < 2; ++sub) {
;         const int qg = 64 * qb + 32 * sub + r32;
;         bf16x8 qr[4];
;         { const bf16_t* qsrc = PROJ + (rowb + qg) * LDP + C_SQ + qh * 64 + 8 * hi;
;           const u32x4 x0 = *(const u32x4*)(qsrc), x1 = *(const u32x4*)(qsrc + 16), x2 = *(const u32x4*)(qsrc + 32), x3 = *(const u32x4*)(qsrc + 48);
;           const float* cs = RC + (rowb + qg) * 32 + 8 * hi; const float* sn = RS + (rowb + qg) * 32 + 8 * hi;
.LBB0_273:
	s_ashr_i32 s44, s89, 9
	s_and_b32 s0, s88, 0x7f
	s_bfe_u32 s4, s89, 0x20007
	s_ashr_i32 s45, s44, 31
	s_lshl_b32 s10, s0, 6
	s_lshl_b64 s[90:91], s[44:45], 13
	s_lshl_b32 s5, s4, 6
	s_lshl_b32 s98, s4, 3
	v_readlane_b32 s99, v254, 23
	s_add_i32 s98, s98, s99
	s_lshl_b32 s98, s98, 2
	v_mov_b32_e32 v192, s98
	global_load_dword v192, v192, s[78:79]
	v_add_u32_e32 v194, s10, v114
	v_mov_b32_e32 v195, v83
	v_add_u32_e32 v172, 64, v194
	v_mov_b32_e32 v173, v83
	v_add_u32_e32 v174, 0x80, v194
	v_mov_b32_e32 v175, v83
	v_mov_b32_e32 v101, v83
	s_lshl_b32 s0, s5, 1
	v_cmp_lt_i32_e32 vcc, -1, v194
	v_mov_b32_e32 v176, 0
	v_mov_b32_e32 v177, 0
	v_mov_b32_e32 v178, 0
	v_mov_b32_e32 v179, 0
	s_and_saveexec_b64 s[46:47], vcc
	v_lshl_add_u64 v[188:189], s[90:91], 0, v[194:195]
	v_mov_b64_e32 v[190:191], s[96:97]
	v_mad_u64_u32 v[190:191], s[50:51], v188, s85, v[190:191]
	v_mad_i32_i24 v191, v189, s85, v191
	v_lshl_add_u64 v[188:189], v[190:191], 0, s[0:1]
	v_lshl_add_u64 v[188:189], v[188:189], 0, v[100:101]
	v_add_co_u32_e32 v188, vcc, 0x4000, v188
	s_nop 1
	v_addc_co_u32_e32 v189, vcc, 0, v189, vcc
	global_load_dwordx4 v[176:179], v[188:189], off offset:512
	s_or_b64 exec, exec, s[46:47]
	v_cmp_lt_i32_e32 vcc, -1, v172
	v_mov_b32_e32 v180, 0
	v_mov_b32_e32 v181, 0
	v_mov_b32_e32 v182, 0
	v_mov_b32_e32 v183, 0
	s_and_saveexec_b64 s[46:47], vcc
	v_lshl_add_u64 v[188:189], s[90:91], 0, v[172:173]
	v_mov_b64_e32 v[190:191], s[96:97]
	v_mad_u64_u32 v[190:191], s[50:51], v188, s85, v[190:191]
	v_mad_i32_i24 v191, v189, s85, v191
	v_lshl_add_u64 v[188:189], v[190:191], 0, s[0:1]
	v_lshl_add_u64 v[188:189], v[188:189], 0, v[100:101]
	v_add_co_u32_e32 v188, vcc, 0x4000, v188
	s_nop 1
	v_addc_co_u32_e32 v189, vcc, 0, v189, vcc
	global_load_dwordx4 v[180:183], v[188:189], off offset:512
	s_or_b64 exec, exec, s[46:47]
	v_cmp_lt_i32_e32 vcc, -1, v174
	v_mov_b32_e32 v184, 0
	v_mov_b32_e32 v185, 0
	v_mov_b32_e32 v186, 0
	v_mov_b32_e32 v187, 0
	s_and_saveexec_b64 s[46:47], vcc
	v_lshl_add_u64 v[188:189], s[90:91], 0, v[174:175]
	v_mov_b64_e32 v[190:191], s[96:97]
	v_mad_u64_u32 v[190:191], s[50:51], v188, s85, v[190:191]
	v_mad_i32_i24 v191, v189, s85, v191
	v_lshl_add_u64 v[188:189], v[190:191], 0, s[0:1]
	v_lshl_add_u64 v[188:189], v[188:189], 0, v[100:101]
	v_add_co_u32_e32 v188, vcc, 0x4000, v188
	s_nop 1
	v_addc_co_u32_e32 v189, vcc, 0, v189, vcc
	global_load_dwordx4 v[184:187], v[188:189], off offset:512
	s_or_b64 exec, exec, s[46:47]
	s_and_b32 s100, s89, 0x7f
	s_lshl_b32 s100, s100, 6
	v_or_b32_e32 v2, s100, v1
	v_or_b32_e32 v6, s90, v2
	v_mov_b64_e32 v[2:3], s[96:97]
	v_mad_u64_u32 v[2:3], s[86:87], v6, s85, v[2:3]
	v_mad_i32_i24 v3, s91, v137, v3
	s_lshl_b32 s0, s98, 5
	v_lshl_add_u64 v[2:3], v[2:3], 0, s[0:1]
	v_lshl_add_u64 v[8:9], v[2:3], 0, v[82:83]
	s_mov_b64 s[86:87], 0x3000
	v_lshl_add_u64 v[10:11], v[8:9], 0, s[86:87]
	v_mov_b32_e32 v7, s91
	s_movk_i32 s86, 0x3000
	v_lshlrev_b64 v[14:15], 7, v[6:7]
	v_add_co_u32_e32 v6, vcc, s86, v8
	global_load_dwordx4 v[40:43], v[10:11], off offset:64
	global_load_dwordx4 v[2:5], v[10:11], off offset:32
	v_addc_co_u32_e32 v7, vcc, 0, v9, vcc
	global_load_dwordx4 v[16:19], v[10:11], off offset:96
	global_load_dwordx4 v[36:39], v[6:7], off
	v_lshl_add_u64 v[20:21], v[90:91], 0, v[14:15]
	global_load_dwordx4 v[10:13], v[20:21], off
	global_load_dwordx4 v[6:9], v[20:21], off offset:16
	global_load_dwordx4 v[28:31], v[20:21], off offset:64
	v_lshl_add_u64 v[14:15], v[88:89], 0, v[14:15]
	global_load_dwordx4 v[44:47], v[14:15], off
	global_load_dwordx4 v[48:51], v[14:15], off offset:16
	global_load_dwordx4 v[32:35], v[14:15], off offset:64
	global_load_dwordx4 v[24:27], v[20:21], off offset:80
	s_nop 0
	global_load_dwordx4 v[20:23], v[14:15], off offset:80
	s_mov_b64 s[44:45], exec
	v_readlane_b32 s46, v254, 56
	v_readlane_b32 s47, v254, 57
	s_and_b64 s[46:47], s[44:45], s[46:47]
	s_mov_b64 exec, s[46:47]
	s_cbranch_execz .LBB0_278
	v_add_u32_e32 v210, s10, v111
	s_mov_b64 s[46:47], 0
	v_mov_b32_e32 v212, v113
	v_mov_b32_e32 v213, v112
	s_branch .LBB0_276
; #define LAS __attribute__((address_space(3)))
; __device__ __forceinline__ unsigned cvtpk(float lo, float hi) { f32x2 v = {lo, hi}; bf16x2_t b = __builtin_convertvector(v, bf16x2_t); return __builtin_bit_cast(unsigned, b); }
; __device__ __forceinline__ void rot8(const u32x4 x1, const u32x4 x2, const f32x4 c0, const f32x4 c1, const f32x4 s0, const f32x4 s1, float sc, u32x4& o1, u32x4& o2) {
;     const unsigned a[4] = {x1.x, x1.y, x1.z, x1.w}, b[4] = {x2.x, x2.y, x2.z, x2.w};
;     const float c[8] = {c0.x, c0.y, c0.z, c0.w, c1.x, c1.y, c1.z, c1.w}, s[8] = {s0.x, s0.y, s0.z, s0.w, s1.x, s1.y, s1.z, s1.w};
;     unsigned r1[4], r2[4];
; #pragma unroll
;     for (int j = 0; j < 4; ++j) { const float a0 = bflo(a[j]), a1 = bfhi(a[j]), b0 = bflo(b[j]), b1 = bfhi(b[j]);
;         r1[j] = cvtpk((a0 * c[2 * j] - b0 * s[2 * j]) * sc, (a1 * c[2 * j + 1] - b1 * s[2 * j + 1]) * sc);
;         r2[j] = cvtpk((b0 * c[2 * j] + a0 * s[2 * j]) * sc, (b1 * c[2 * j + 1] + a1 * s[2 * j + 1]) * sc); }
;     o1 = (u32x4){r1[0], r1[1], r1[2], r1[3]}; o2 = (u32x4){r2[0], r2[1], r2[2], r2[3]};
; __device__ __forceinline__ void swa_unit(Frame& F, int b, int kvh, int qb) {
;     ...
;     for (int task = tid; task < 768; task += NTHREADS) { const int key = task >> 2, c = task & 3, kg = K0 + key;
;         u32x4 o1 = (u32x4){0u, 0u, 0u, 0u}, o2 = o1;
;         if (kg >= 0) { const bf16_t* src = PROJ + (rowb + kg) * LDP + C_SK + kvh * 64; const u32x4 x1 = *(const u32x4*)(src + 8 * c), x2 = *(const u32x4*)(src + 32 + 8 * c);
;             const float* cs = RC + (rowb + kg) * 32 + 8 * c; const float* sn = RS + (rowb + kg) * 32 + 8 * c;
;             rot8(x1, x2, *(const f32x4*)cs, *(const f32x4*)(cs + 4), *(const f32x4*)sn, *(const f32x4*)(sn + 4), 1.0f, o1, o2); }
;         *(LAS u32x4*)(Kl + key * SWA_KROW + 16 * c) = o1; *(LAS u32x4*)(Kl + key * SWA_KROW + 64 + 16 * c) = o2; }
.LBB0_275:
	s_or_b64 exec, exec, s[48:49]
	v_add_u32_e32 v212, 0x200, v212
	s_movk_i32 s0, 0xff
	v_cmp_lt_u32_e32 vcc, s0, v212
	ds_write_b128 v213, v[206:209]
	ds_write_b128 v213, v[202:205] offset:64
	v_add_u32_e32 v210, 0x80, v210
	s_or_b64 s[46:47], vcc, s[46:47]
	v_add_u32_e32 v213, 0x4800, v213
	s_andn2_b64 exec, exec, s[46:47]
	s_cbranch_execz .LBB0_278
.LBB0_276:
	v_cmp_lt_i32_e32 vcc, -1, v210
	v_mov_b32_e32 v202, 0
	v_mov_b32_e32 v203, 0
	v_mov_b32_e32 v204, 0
	v_mov_b32_e32 v205, 0
	v_mov_b32_e32 v206, 0
	v_mov_b32_e32 v207, 0
	v_mov_b32_e32 v208, 0
	v_mov_b32_e32 v209, 0
	s_and_saveexec_b64 s[48:49], vcc
	s_cbranch_execz .LBB0_275
	v_mov_b32_e32 v211, v83
	v_lshl_add_u64 v[214:215], s[90:91], 0, v[210:211]
	v_mov_b64_e32 v[202:203], s[96:97]
	v_mad_u64_u32 v[202:203], s[50:51], v214, s85, v[202:203]
	v_mad_i32_i24 v203, v215, s85, v203
	s_lshl_b32 s0, s5, 1
	v_lshl_add_u64 v[202:203], v[202:203], 0, s[0:1]
	v_mov_b32_e32 v99, v83
	v_lshl_add_u64 v[202:203], v[202:203], 0, v[98:99]
	s_mov_b64 s[50:51], 0x4000
	s_movk_i32 s0, 0x4000
	v_lshl_add_u64 v[206:207], v[202:203], 0, s[50:51]
	v_add_co_u32_e32 v202, vcc, s0, v202
	v_lshlrev_b64 v[214:215], 7, v[214:215]
	s_nop 0
	v_addc_co_u32_e32 v203, vcc, 0, v203, vcc
	global_load_dwordx4 v[202:205], v[202:203], off
	s_nop 0
	global_load_dwordx4 v[206:209], v[206:207], off offset:64
	v_lshl_add_u64 v[218:219], v[84:85], 0, v[214:215]
	v_lshl_add_u64 v[226:227], v[86:87], 0, v[214:215]
	global_load_dwordx4 v[214:217], v[218:219], off offset:16
	s_nop 0
	global_load_dwordx4 v[218:221], v[218:219], off
	s_nop 0
	global_load_dwordx4 v[222:225], v[226:227], off offset:16
	s_nop 0
	global_load_dwordx4 v[226:229], v[226:227], off
	s_waitcnt vmcnt(0)
	v_lshlrev_b32_e32 v230, 16, v202
	v_and_b32_e32 v231, 0xffff0000, v202
	v_lshlrev_b32_e32 v232, 16, v206
	v_and_b32_e32 v233, 0xffff0000, v206
	v_pk_mul_f32 v[234:235], v[226:227], v[232:233]
	v_pk_mul_f32 v[226:227], v[226:227], v[230:231]
	v_pk_fma_f32 v[234:235], v[218:219], v[230:231], v[234:235] neg_lo:[0,0,1] neg_hi:[0,0,1]
	v_pk_fma_f32 v[218:219], v[218:219], v[232:233], v[226:227]
	v_lshlrev_b32_e32 v226, 16, v207
	v_and_b32_e32 v227, 0xffff0000, v207
	v_cvt_pk_bf16_f32 v202, v218, v219
	v_lshlrev_b32_e32 v218, 16, v203
	v_and_b32_e32 v219, 0xffff0000, v203
	v_pk_mul_f32 v[230:231], v[228:229], v[226:227]
	v_cvt_pk_bf16_f32 v206, v234, v235
	v_pk_fma_f32 v[230:231], v[220:221], v[218:219], v[230:231] neg_lo:[0,0,1] neg_hi:[0,0,1]
	v_pk_mul_f32 v[218:219], v[228:229], v[218:219]
	v_cvt_pk_bf16_f32 v207, v230, v231
	v_pk_fma_f32 v[218:219], v[220:221], v[226:227], v[218:219]
	v_lshlrev_b32_e32 v220, 16, v208
	v_and_b32_e32 v221, 0xffff0000, v208
	v_cvt_pk_bf16_f32 v203, v218, v219
	v_lshlrev_b32_e32 v218, 16, v204
	v_and_b32_e32 v219, 0xffff0000, v204
	v_pk_mul_f32 v[226:227], v[222:223], v[220:221]
	s_nop 0
	v_pk_fma_f32 v[226:227], v[214:215], v[218:219], v[226:227] neg_lo:[0,0,1] neg_hi:[0,0,1]
	v_pk_mul_f32 v[218:219], v[222:223], v[218:219]
	v_cvt_pk_bf16_f32 v208, v226, v227
	v_pk_fma_f32 v[214:215], v[214:215], v[220:221], v[218:219]
	v_lshlrev_b32_e32 v218, 16, v209
	v_and_b32_e32 v219, 0xffff0000, v209
	v_cvt_pk_bf16_f32 v204, v214, v215
	v_lshlrev_b32_e32 v214, 16, v205
	v_and_b32_e32 v215, 0xffff0000, v205
	v_pk_mul_f32 v[220:221], v[224:225], v[218:219]
	s_nop 0
	v_pk_fma_f32 v[220:221], v[216:217], v[214:215], v[220:221] neg_lo:[0,0,1] neg_hi:[0,0,1]
	v_pk_mul_f32 v[214:215], v[224:225], v[214:215]
	v_cvt_pk_bf16_f32 v209, v220, v221
	v_pk_fma_f32 v[214:215], v[216:217], v[218:219], v[214:215]
	s_nop 0
	v_cvt_pk_bf16_f32 v205, v214, v215
	s_branch .LBB0_275

; __device__ __forceinline__ void swa_unit(Frame& F, int b, int kvh, int qb) {
;     ...
;     __syncthreads();
;     const int qh = kvh * 8 + F.wave;
;     const float sink2 = F.sinks[qh] * 1.4426950408889634f;
; #pragma unroll 1
;     for (int sub = 0; sub < 2; ++sub) {
;         const int qg = 64 * qb + 32 * sub + r32;
.LBB0_282:
	s_lshl_b32 s0, s4, 3
	v_readlane_b32 s4, v254, 23
	s_add_i32 s0, s0, s4
	s_lshl_b32 s4, s0, 2
	s_waitcnt lgkmcnt(0)
	s_barrier
	s_and_b32 s10, s89, 0x7f
	v_readlane_b32 s5, v254, 24
	s_lshl_b32 s84, s10, 6
	s_add_i32 s4, s84, 0xffffff80
	s_lshl_b32 s5, s0, 6
	s_cmp_gt_u32 s10, 1
	v_readlane_b32 s46, v254, 58
	s_cselect_b64 s[74:75], -1, 0
	v_readlane_b32 s47, v254, 59
	s_mov_b32 s11, 0
	s_and_b64 s[44:45], s[74:75], s[8:9]
	s_and_b64 s[46:47], s[74:75], s[46:47]
	s_and_b64 s[48:49], s[74:75], s[12:13]
	s_and_b64 s[50:51], s[74:75], s[14:15]
	s_and_b64 s[52:53], s[74:75], s[16:17]
	s_and_b64 s[54:55], s[74:75], s[18:19]
	s_and_b64 s[56:57], s[74:75], s[20:21]
	s_and_b64 s[58:59], s[74:75], s[22:23]
	s_and_b64 s[60:61], s[74:75], s[24:25]
	s_and_b64 s[62:63], s[74:75], s[26:27]
	s_and_b64 s[64:65], s[74:75], s[28:29]
	s_and_b64 s[66:67], s[74:75], s[30:31]
	s_and_b64 s[68:69], s[74:75], s[34:35]
	s_and_b64 s[70:71], s[74:75], s[36:37]
	s_and_b64 s[72:73], s[74:75], s[38:39]
	s_and_b64 s[74:75], s[74:75], s[40:41]
	s_mov_b64 s[94:95], -1
	s_mov_b32 s10, s84
	v_mul_f32_e32 v99, 0x3fb8aa3b, v192
	s_lshl_b32 s0, s5, 1
	s_branch .Lswa_first

; #define LAS __attribute__((address_space(3)))
; __device__ __forceinline__ void rot8(const u32x4 x1, const u32x4 x2, const f32x4 c0, const f32x4 c1, const f32x4 s0, const f32x4 s1, float sc, u32x4& o1, u32x4& o2) {
;     const unsigned a[4] = {x1.x, x1.y, x1.z, x1.w}, b[4] = {x2.x, x2.y, x2.z, x2.w};
;     const float c[8] = {c0.x, c0.y, c0.z, c0.w, c1.x, c1.y, c1.z, c1.w}, s[8] = {s0.x, s0.y, s0.z, s0.w, s1.x, s1.y, s1.z, s1.w};
;     unsigned r1[4], r2[4];
; #pragma unroll
;     for (int j = 0; j < 4; ++j) { const float a0 = bflo(a[j]), a1 = bfhi(a[j]), b0 = bflo(b[j]), b1 = bfhi(b[j]);
;         r1[j] = cvtpk((a0 * c[2 * j] - b0 * s[2 * j]) * sc, (a1 * c[2 * j + 1] - b1 * s[2 * j + 1]) * sc);
;         r2[j] = cvtpk((b0 * c[2 * j] + a0 * s[2 * j]) * sc, (b1 * c[2 * j + 1] + a1 * s[2 * j + 1]) * sc); }
;     o1 = (u32x4){r1[0], r1[1], r1[2], r1[3]}; o2 = (u32x4){r2[0], r2[1], r2[2], r2[3]};
; __device__ __forceinline__ void swa_unit(Frame& F, int b, int kvh, int qb) {
;     ...
;         { const bf16_t* qsrc = PROJ + (rowb + qg) * LDP + C_SQ + qh * 64 + 8 * hi;
;           const u32x4 x0 = *(const u32x4*)(qsrc), x1 = *(const u32x4*)(qsrc + 16), x2 = *(const u32x4*)(qsrc + 32), x3 = *(const u32x4*)(qsrc + 48);
;           const float* cs = RC + (rowb + qg) * 32 + 8 * hi; const float* sn = RS + (rowb + qg) * 32 + 8 * hi;
;           u32x4 o0, o1, o2, o3; const float sc = 0.125f * 1.4426950408889634f;
;           rot8(x0, x2, *(const f32x4*)cs, *(const f32x4*)(cs + 4), *(const f32x4*)sn, *(const f32x4*)(sn + 4), sc, o0, o2);
;           rot8(x1, x3, *(const f32x4*)(cs + 16), *(const f32x4*)(cs + 20), *(const f32x4*)(sn + 16), *(const f32x4*)(sn + 20), sc, o1, o3);
;           qr[0] = __builtin_bit_cast(bf16x8, o0); qr[1] = __builtin_bit_cast(bf16x8, o1); qr[2] = __builtin_bit_cast(bf16x8, o2); qr[3] = __builtin_bit_cast(bf16x8, o3); }
;         f32x16 p[5];
; #pragma unroll
;         for (int j = 0; j < 5; ++j) {
; #pragma unroll
;             for (int r = 0; r < 16; ++r) p[j][r] = 0.f;
; #pragma unroll
;             for (int d0 = 0; d0 < 4; ++d0) { const bf16x8 kf = *(const LAS bf16x8*)(Kl + (32 * sub + 32 * j + r32) * SWA_KROW + (16 * d0 + 8 * hi) * 2);
;                 p[j] = __builtin_amdgcn_mfma_f32_32x32x16_bf16(kf, qr[d0], p[j], 0, 0, 0); } }
.Lswa_first:
	s_or_b32 s86, s11, s4
	s_cmpk_gt_i32 s86, 0xffdf
	s_cselect_b64 vcc, -1, 0
	s_cmpk_gt_i32 s86, 0xffbf
	s_waitcnt vmcnt(11)
	v_lshlrev_b32_e32 v14, 16, v40
	v_and_b32_e32 v15, 0xffff0000, v40
	v_lshlrev_b32_e32 v52, 16, v41
	v_and_b32_e32 v53, 0xffff0000, v41
	v_lshlrev_b32_e32 v54, 16, v42
	v_and_b32_e32 v55, 0xffff0000, v42
	v_lshlrev_b32_e32 v56, 16, v43
	v_and_b32_e32 v57, 0xffff0000, v43
	s_waitcnt vmcnt(10)
	v_lshlrev_b32_e32 v58, 16, v2
	v_and_b32_e32 v59, 0xffff0000, v2
	s_waitcnt vmcnt(9)
	v_lshlrev_b32_e32 v60, 16, v16
	v_and_b32_e32 v61, 0xffff0000, v16
	v_lshlrev_b32_e32 v40, 16, v3
	v_and_b32_e32 v41, 0xffff0000, v3
	v_lshlrev_b32_e32 v42, 16, v17
	v_and_b32_e32 v43, 0xffff0000, v17
	s_waitcnt vmcnt(8)
	v_lshlrev_b32_e32 v2, 16, v36
	v_and_b32_e32 v3, 0xffff0000, v36
	s_waitcnt vmcnt(7)
	v_pk_mul_f32 v[16:17], v[10:11], v[14:15]
	v_lshlrev_b32_e32 v64, 16, v38
	s_waitcnt vmcnt(4)
	v_pk_fma_f32 v[16:17], v[44:45], v[2:3], v[16:17] neg_lo:[0,0,1] neg_hi:[0,0,1]
	v_pk_mul_f32 v[2:3], v[10:11], v[2:3]
	v_and_b32_e32 v65, 0xffff0000, v38
	v_pk_fma_f32 v[2:3], v[44:45], v[14:15], v[2:3]
	v_lshlrev_b32_e32 v38, 16, v39
	v_pk_mul_f32 v[2:3], v[2:3], s[92:93] op_sel_hi:[1,0]
	v_and_b32_e32 v39, 0xffff0000, v39
	v_cvt_pk_bf16_f32 v144, v2, v3
	v_pk_mul_f32 v[2:3], v[30:31], v[42:43]
	v_pk_mul_f32 v[66:67], v[6:7], v[54:55]
	s_waitcnt vmcnt(2)
	v_pk_fma_f32 v[2:3], v[34:35], v[40:41], v[2:3] neg_lo:[0,0,1] neg_hi:[0,0,1]
	v_pk_mul_f32 v[68:69], v[8:9], v[56:57]
	v_pk_mul_f32 v[6:7], v[6:7], v[64:65]
	v_pk_mul_f32 v[8:9], v[8:9], v[38:39]
	v_pk_mul_f32 v[2:3], v[2:3], s[92:93] op_sel_hi:[1,0]
	v_pk_fma_f32 v[6:7], v[48:49], v[54:55], v[6:7]
	v_pk_fma_f32 v[8:9], v[50:51], v[56:57], v[8:9]
	v_cvt_pk_bf16_f32 v141, v2, v3
	v_or_b32_e32 v2, s11, v1
	v_pk_mul_f32 v[6:7], v[6:7], s[92:93] op_sel_hi:[1,0]
	v_pk_mul_f32 v[8:9], v[8:9], s[92:93] op_sel_hi:[1,0]
	v_mad_u32_u24 v101, v2, s3, v93
	v_cvt_pk_bf16_f32 v146, v6, v7
	v_cvt_pk_bf16_f32 v147, v8, v9
	ds_read_b128 v[6:9], v101
	v_lshlrev_b32_e32 v36, 16, v37
	v_and_b32_e32 v37, 0xffff0000, v37
	v_pk_mul_f32 v[62:63], v[12:13], v[52:53]
	v_pk_mul_f32 v[70:71], v[28:29], v[60:61]
	v_pk_mul_f32 v[28:29], v[28:29], v[58:59]
	v_pk_fma_f32 v[10:11], v[46:47], v[36:37], v[62:63] neg_lo:[0,0,1] neg_hi:[0,0,1]
	v_pk_fma_f32 v[62:63], v[50:51], v[38:39], v[68:69] neg_lo:[0,0,1] neg_hi:[0,0,1]
	v_pk_mul_f32 v[12:13], v[12:13], v[36:37]
	v_pk_fma_f32 v[36:37], v[48:49], v[64:65], v[66:67] neg_lo:[0,0,1] neg_hi:[0,0,1]
	v_pk_fma_f32 v[38:39], v[32:33], v[58:59], v[70:71] neg_lo:[0,0,1] neg_hi:[0,0,1]
	v_pk_fma_f32 v[28:29], v[32:33], v[60:61], v[28:29]
	v_pk_mul_f32 v[32:33], v[62:63], s[92:93] op_sel_hi:[1,0]
	v_lshlrev_b32_e32 v48, 16, v18
	v_and_b32_e32 v49, 0xffff0000, v18
	v_cvt_pk_bf16_f32 v69, v32, v33
	v_lshlrev_b32_e32 v32, 16, v4
	v_and_b32_e32 v33, 0xffff0000, v4
	s_waitcnt vmcnt(1)
	v_pk_mul_f32 v[2:3], v[24:25], v[48:49]
	v_pk_mul_f32 v[16:17], v[16:17], s[92:93] op_sel_hi:[1,0]
	v_pk_mul_f32 v[10:11], v[10:11], s[92:93] op_sel_hi:[1,0]
	v_pk_fma_f32 v[12:13], v[46:47], v[52:53], v[12:13]
	v_pk_mul_f32 v[14:15], v[36:37], s[92:93] op_sel_hi:[1,0]
	v_pk_mul_f32 v[36:37], v[38:39], s[92:93] op_sel_hi:[1,0]
	s_waitcnt vmcnt(0)
	v_pk_fma_f32 v[2:3], v[20:21], v[32:33], v[2:3] neg_lo:[0,0,1] neg_hi:[0,0,1]
	v_cvt_pk_bf16_f32 v66, v16, v17
	v_cvt_pk_bf16_f32 v67, v10, v11
	v_pk_mul_f32 v[10:11], v[12:13], s[92:93] op_sel_hi:[1,0]
	v_cvt_pk_bf16_f32 v68, v14, v15
	v_cvt_pk_bf16_f32 v140, v36, v37
	v_pk_mul_f32 v[2:3], v[2:3], s[92:93] op_sel_hi:[1,0]
	ds_read_b128 v[36:39], v101 offset:32
	v_cvt_pk_bf16_f32 v145, v10, v11
	v_cvt_pk_bf16_f32 v142, v2, v3
	v_lshlrev_b32_e32 v50, 16, v5
	v_and_b32_e32 v51, 0xffff0000, v5
	s_waitcnt lgkmcnt(1)
	v_mfma_f32_32x32x16_bf16 v[2:17], v[6:9], v[66:69], 0
	v_lshlrev_b32_e32 v18, 16, v19
	v_and_b32_e32 v19, 0xffff0000, v19
	v_mul_f32_e64 v44, v26, v18
	v_mul_f32_e64 v45, v27, v19
	v_mul_f32_e64 v24, v24, v32
	v_mul_f32_e64 v25, v25, v33
	v_pk_fma_f32 v[44:45], v[22:23], v[50:51], v[44:45] neg_lo:[0,0,1] neg_hi:[0,0,1]
	v_pk_fma_f32 v[20:21], v[20:21], v[48:49], v[24:25]
	v_pk_mul_f32 v[44:45], v[44:45], s[92:93] op_sel_hi:[1,0]
	v_pk_mul_f32 v[20:21], v[20:21], s[92:93] op_sel_hi:[1,0]
	v_cvt_pk_bf16_f32 v143, v44, v45
	ds_read_b128 v[44:47], v101 offset:64
	v_cvt_pk_bf16_f32 v150, v20, v21
	s_waitcnt lgkmcnt(1)
	v_mfma_f32_32x32x16_bf16 v[2:17], v[36:39], v[140:143], v[2:17]
	v_mul_f32_e64 v20, v26, v50
	v_mul_f32_e64 v21, v27, v51
	v_mul_f32_e64 v28, v28, s92
	v_mul_f32_e64 v29, v29, s92
	v_fma_f32 v18, v22, v18, v20
	v_fma_f32 v19, v23, v19, v21
	v_cvt_pk_bf16_f32 v148, v28, v29
	v_pk_mul_f32 v[28:29], v[30:31], v[40:41]
	v_pk_mul_f32 v[18:19], v[18:19], s[92:93] op_sel_hi:[1,0]
	v_pk_fma_f32 v[28:29], v[34:35], v[42:43], v[28:29]
	v_cvt_pk_bf16_f32 v151, v18, v19
	v_add_u32_e32 v18, s11, v108
	v_pk_mul_f32 v[28:29], v[28:29], s[92:93] op_sel_hi:[1,0]
	v_mad_u32_u24 v38, v18, s3, v93
	v_cvt_pk_bf16_f32 v149, v28, v29
	ds_read_b128 v[28:31], v101 offset:96
	ds_read_b128 v[18:21], v38
	ds_read_b128 v[34:37], v38 offset:32
	s_waitcnt lgkmcnt(3)
	v_mfma_f32_32x32x16_bf16 v[2:17], v[44:47], v[144:147], v[2:17]
	ds_read_b128 v[50:53], v101 offset:9248
	ds_read_b128 v[156:159], v101 offset:18464
	s_waitcnt lgkmcnt(4)
	v_mfma_f32_32x32x16_bf16 v[2:17], v[28:31], v[148:151], v[2:17]
	s_waitcnt lgkmcnt(3)
	v_mfma_f32_32x32x16_bf16 v[18:33], v[18:21], v[66:69], 0
	s_nop 9
	v_cndmask_b32_e64 v3, v138, v3, s[46:47]
	v_cndmask_b32_e64 v4, v138, v4, s[48:49]
	v_cndmask_b32_e64 v5, v138, v5, s[50:51]
	v_cndmask_b32_e64 v6, v138, v6, s[52:53]
	v_cndmask_b32_e64 v7, v138, v7, s[54:55]
	v_cndmask_b32_e64 v8, v138, v8, s[56:57]
	v_cndmask_b32_e64 v9, v138, v9, s[58:59]
	s_waitcnt lgkmcnt(2)
; #define LAS __attribute__((address_space(3)))
; __device__ __forceinline__ int crow(int r, int hi) { return (r & 3) + 8 * (r >> 2) + 4 * hi; }
; __device__ __forceinline__ void swa_unit(Frame& F, int b, int kvh, int qb) {
;     ...
;             for (int d0 = 0; d0 < 4; ++d0) { const bf16x8 kf = *(const LAS bf16x8*)(Kl + (32 * sub + 32 * j + r32) * SWA_KROW + (16 * d0 + 8 * hi) * 2);
;                 p[j] = __builtin_amdgcn_mfma_f32_32x32x16_bf16(kf, qr[d0], p[j], 0, 0, 0); } }
;         const int kneg = -(K0 + 32 * sub);
;         const float NEG = -INFINITY;
; #pragma unroll
;         for (int j = 0; j < 5; ++j)
; #pragma unroll
;             for (int r = 0; r < 16; ++r) { const int c = crow(r, hi); bool ok = (32 * j >= kneg);
;                 if (j == 0) ok = ok && (c > r32); if (j == 4) ok = ok && (c <= r32);
;                 p[j][r] = ok ? p[j][r] : NEG; }
;         float mx = sink2;
; #pragma unroll
;         for (int j = 0; j < 5; ++j)
; #pragma unroll
;             for (int r = 0; r < 16; ++r) mx = fmaxf(mx, p[j][r]);
;         mx = fmaxf(mx, __shfl_xor(mx, 32));
	v_mfma_f32_32x32x16_bf16 v[18:33], v[34:37], v[140:143], v[18:33]
	ds_read_b128 v[34:37], v38 offset:64
	v_cndmask_b32_e64 v10, v138, v10, s[60:61]
	v_cndmask_b32_e64 v11, v138, v11, s[62:63]
	v_cndmask_b32_e64 v12, v138, v12, s[64:65]
	v_cndmask_b32_e64 v13, v138, v13, s[66:67]
	v_cndmask_b32_e64 v14, v138, v14, s[68:69]
	v_cndmask_b32_e64 v15, v138, v15, s[70:71]
	s_waitcnt lgkmcnt(0)
	v_mfma_f32_32x32x16_bf16 v[18:33], v[34:37], v[144:147], v[18:33]
	ds_read_b128 v[34:37], v38 offset:96
	v_cndmask_b32_e64 v16, v138, v16, s[72:73]
	v_cndmask_b32_e64 v17, v138, v17, s[74:75]
	s_waitcnt lgkmcnt(0)
	v_mfma_f32_32x32x16_bf16 v[18:33], v[34:37], v[148:151], v[18:33]
	ds_read_b128 v[34:37], v101 offset:9216
	s_waitcnt lgkmcnt(0)
	v_mfma_f32_32x32x16_bf16 v[34:49], v[34:37], v[66:69], 0
	s_nop 8
	v_cndmask_b32_e32 v20, v138, v20, vcc
	v_cndmask_b32_e32 v21, v138, v21, vcc
	v_cndmask_b32_e32 v22, v138, v22, vcc
	v_cndmask_b32_e32 v23, v138, v23, vcc
	v_cndmask_b32_e32 v24, v138, v24, vcc
	v_cndmask_b32_e32 v25, v138, v25, vcc
	v_cndmask_b32_e32 v26, v138, v26, vcc
	v_mfma_f32_32x32x16_bf16 v[34:49], v[50:53], v[140:143], v[34:49]
	ds_read_b128 v[50:53], v101 offset:9280
	v_cndmask_b32_e32 v27, v138, v27, vcc
	v_cndmask_b32_e32 v28, v138, v28, vcc
	v_cndmask_b32_e32 v29, v138, v29, vcc
	v_cndmask_b32_e32 v30, v138, v30, vcc
	v_cndmask_b32_e32 v31, v138, v31, vcc
	v_cndmask_b32_e32 v32, v138, v32, vcc
	s_waitcnt lgkmcnt(0)
	v_mfma_f32_32x32x16_bf16 v[34:49], v[50:53], v[144:147], v[34:49]
	ds_read_b128 v[50:53], v101 offset:9312
	v_cndmask_b32_e32 v33, v138, v33, vcc
	s_waitcnt lgkmcnt(0)
	v_mfma_f32_32x32x16_bf16 v[34:49], v[50:53], v[148:151], v[34:49]
	v_add_u32_e32 v50, s11, v109
	v_mad_u32_u24 v74, v50, s3, v93
	ds_read_b128 v[50:53], v74
	ds_read_b128 v[70:73], v74 offset:32
	s_waitcnt lgkmcnt(1)
	v_mfma_f32_32x32x16_bf16 v[50:65], v[50:53], v[66:69], 0
	s_waitcnt lgkmcnt(0)
	v_mfma_f32_32x32x16_bf16 v[50:65], v[70:73], v[140:143], v[50:65]
	ds_read_b128 v[70:73], v74 offset:64
	s_waitcnt lgkmcnt(0)
	v_mfma_f32_32x32x16_bf16 v[50:65], v[70:73], v[144:147], v[50:65]
	ds_read_b128 v[70:73], v74 offset:96
	s_waitcnt lgkmcnt(0)
	v_mfma_f32_32x32x16_bf16 v[50:65], v[70:73], v[148:151], v[50:65]
	ds_read_b128 v[70:73], v101 offset:18432
	s_waitcnt lgkmcnt(0)
	v_mfma_f32_32x32x16_bf16 v[66:81], v[70:73], v[66:69], 0
	v_mfma_f32_32x32x16_bf16 v[66:81], v[156:159], v[140:143], v[66:81]
	ds_read_b128 v[140:143], v101 offset:18496
	s_waitcnt lgkmcnt(0)
	v_mfma_f32_32x32x16_bf16 v[66:81], v[140:143], v[144:147], v[66:81]
	ds_read_b128 v[140:143], v101 offset:18528
	s_waitcnt lgkmcnt(0)
	v_mfma_f32_32x32x16_bf16 v[66:81], v[140:143], v[148:151], v[66:81]
	v_cndmask_b32_e64 v140, v138, v2, s[44:45]
	v_cndmask_b32_e32 v141, v138, v18, vcc
	v_cndmask_b32_e32 v142, v138, v19, vcc
	s_cselect_b64 vcc, -1, 0
	v_cndmask_b32_e32 v151, v138, v42, vcc
	v_max3_f32 v42, v99, v140, v3
	v_max3_f32 v42, v42, v4, v5
	v_max3_f32 v42, v42, v6, v7
	v_max3_f32 v42, v42, v8, v9
	v_max3_f32 v42, v42, v10, v11
	v_max3_f32 v42, v42, v12, v13
	v_max3_f32 v42, v42, v14, v15
	v_max3_f32 v42, v42, v16, v17
	v_max3_f32 v42, v42, v141, v142
	v_max3_f32 v42, v42, v20, v21
	v_max3_f32 v42, v42, v22, v23
	v_max3_f32 v42, v42, v24, v25
	v_max3_f32 v42, v42, v26, v27
	v_max3_f32 v42, v42, v28, v29
	v_max3_f32 v42, v42, v30, v31
	v_cndmask_b32_e32 v143, v138, v34, vcc
	v_cndmask_b32_e32 v144, v138, v35, vcc
	v_max3_f32 v42, v42, v32, v33
	v_cndmask_b32_e32 v145, v138, v36, vcc
	v_cndmask_b32_e32 v146, v138, v37, vcc
	v_max3_f32 v42, v42, v143, v144
	v_cndmask_b32_e32 v147, v138, v38, vcc
	v_cndmask_b32_e32 v148, v138, v39, vcc
	v_max3_f32 v42, v42, v145, v146
	v_cndmask_b32_e32 v149, v138, v40, vcc
	v_cndmask_b32_e32 v150, v138, v41, vcc
	v_max3_f32 v42, v42, v147, v148
	v_cndmask_b32_e32 v152, v138, v43, vcc
	v_max3_f32 v42, v42, v149, v150
	v_cndmask_b32_e32 v153, v138, v44, vcc
	v_cndmask_b32_e32 v155, v138, v45, vcc
	v_max3_f32 v42, v42, v151, v152
	v_cndmask_b32_e32 v46, v138, v46, vcc
	v_cndmask_b32_e32 v156, v138, v47, vcc
	s_cmpk_gt_i32 s86, 0xff9f
	v_max3_f32 v42, v42, v153, v155
	v_cndmask_b32_e32 v157, v138, v48, vcc
	v_cndmask_b32_e32 v158, v138, v49, vcc
	s_cselect_b64 vcc, -1, 0
	v_max3_f32 v42, v42, v46, v156
	v_cndmask_b32_e32 v159, v138, v50, vcc
	v_cndmask_b32_e32 v160, v138, v51, vcc
	v_max3_f32 v42, v42, v157, v158
	v_cndmask_b32_e32 v161, v138, v52, vcc
	v_cndmask_b32_e32 v2, v138, v53, vcc
	v_max3_f32 v42, v42, v159, v160
	v_cndmask_b32_e32 v19, v138, v54, vcc
	v_cndmask_b32_e32 v18, v138, v55, vcc
	v_max3_f32 v42, v42, v161, v2
	v_cndmask_b32_e32 v139, v138, v56, vcc
	v_cndmask_b32_e32 v103, v138, v57, vcc
	v_max3_f32 v42, v42, v19, v18
	v_cndmask_b32_e32 v101, v138, v58, vcc
	v_cndmask_b32_e32 v58, v138, v59, vcc
	v_max3_f32 v42, v42, v139, v103
	v_cndmask_b32_e32 v57, v138, v60, vcc
	v_cndmask_b32_e32 v56, v138, v61, vcc
	v_max3_f32 v42, v42, v101, v58
	v_cndmask_b32_e32 v55, v138, v62, vcc
	v_cndmask_b32_e32 v54, v138, v63, vcc
	v_max3_f32 v42, v42, v57, v56
	v_cndmask_b32_e32 v53, v138, v64, vcc
	v_cndmask_b32_e32 v52, v138, v65, vcc
	v_max3_f32 v42, v42, v55, v54
	v_cndmask_b32_e64 v51, v66, v138, s[8:9]
	v_cndmask_b32_e64 v50, v138, v67, s[42:43]
	v_max3_f32 v42, v42, v53, v52
	v_cndmask_b32_e64 v49, v68, v138, s[12:13]
	v_cndmask_b32_e64 v48, v69, v138, s[14:15]
	v_max3_f32 v42, v42, v51, v50
	v_cndmask_b32_e64 v47, v70, v138, s[16:17]
	v_cndmask_b32_e64 v45, v71, v138, s[18:19]
	v_max3_f32 v42, v42, v49, v48
	v_cndmask_b32_e64 v44, v72, v138, s[20:21]
	v_cndmask_b32_e64 v43, v73, v138, s[22:23]
	v_max3_f32 v42, v42, v47, v45
	v_cndmask_b32_e64 v41, v74, v138, s[24:25]
	v_cndmask_b32_e64 v40, v75, v138, s[26:27]
	v_max3_f32 v42, v42, v44, v43
	v_cndmask_b32_e64 v39, v76, v138, s[28:29]
	v_cndmask_b32_e64 v38, v77, v138, s[30:31]
	v_max3_f32 v42, v42, v41, v40
	v_cndmask_b32_e64 v37, v78, v138, s[34:35]
	v_cndmask_b32_e64 v36, v79, v138, s[36:37]
	v_max3_f32 v42, v42, v39, v38
	v_cndmask_b32_e64 v35, v80, v138, s[38:39]
	v_cndmask_b32_e64 v34, v81, v138, s[40:41]
	v_max3_f32 v42, v42, v37, v36
	v_max3_f32 v42, v42, v35, v34
	ds_bpermute_b32 v59, v110, v42
	s_waitcnt lgkmcnt(0)
; #define LAS __attribute__((address_space(3)))
; __device__ __forceinline__ unsigned cvtpk(float lo, float hi) { f32x2 v = {lo, hi}; bf16x2_t b = __builtin_convertvector(v, bf16x2_t); return __builtin_bit_cast(unsigned, b); }
; __device__ __forceinline__ void swa_unit(Frame& F, int b, int kvh, int qb) {
;     ...
;         mx = fmaxf(mx, __shfl_xor(mx, 32));
;         float sum = 0.f;
; #pragma unroll
;         for (int j = 0; j < 5; ++j)
; #pragma unroll
;             for (int r = 0; r < 16; ++r) { p[j][r] = __builtin_amdgcn_exp2f(p[j][r] - mx); sum += p[j][r]; }
;         sum += __shfl_xor(sum, 32);
;         sum += __builtin_amdgcn_exp2f(sink2 - mx);
;         f32x16 o[2];
; #pragma unroll
;         for (int r = 0; r < 16; ++r) { o[0][r] = 0.f; o[1][r] = 0.f; }
;         const int vrow0 = 32 * sub + 4 * hi + ((lane & 15) >> 2), vcol = ((lane >> 4) & 1) * 32 + (lane & 3) * 8;
; #pragma unroll
;         for (int j = 0; j < 5; ++j)
; #pragma unroll
;             for (int s = 0; s < 2; ++s) {
;                 u32x4 pw; pw.x = cvtpk(p[j][8 * s], p[j][8 * s + 1]); pw.y = cvtpk(p[j][8 * s + 2], p[j][8 * s + 3]); pw.z = cvtpk(p[j][8 * s + 4], p[j][8 * s + 5]); pw.w = cvtpk(p[j][8 * s + 6], p[j][8 * s + 7]);
;                 const bf16x8 pa = __builtin_bit_cast(bf16x8, pw);
; #pragma unroll
;                 for (int d0 = 0; d0 < 2; ++d0) { const LAS unsigned char* vp = Vl + (vrow0 + 32 * j + 16 * s) * SWA_KROW + d0 * 64 + vcol;
;                     const s16x4 lo = __builtin_bit_cast(s16x4, __builtin_amdgcn_ds_read_tr16_b64_v4i16((LAS s16x4*)vp));
;                     const s16x4 hh = __builtin_bit_cast(s16x4, __builtin_amdgcn_ds_read_tr16_b64_v4i16((LAS s16x4*)(vp + 8 * SWA_KROW)));
;                     const bf16x8 vf = (bf16x8){lo[0], lo[1], lo[2], lo[3], hh[0], hh[1], hh[2], hh[3]};
;                     o[d0] = __builtin_amdgcn_mfma_f32_32x32x16_bf16(pa, vf, o[d0], 0, 0, 0); } }
	v_max_f32_e32 v59, v59, v59
	v_max_f32_e32 v42, v42, v59
	v_sub_f32_e32 v59, v140, v42
	v_exp_f32_e32 v59, v59
	v_sub_f32_e32 v3, v3, v42
	v_exp_f32_e32 v3, v3
	v_sub_f32_e32 v4, v4, v42
	v_exp_f32_e32 v4, v4
	v_sub_f32_e32 v5, v5, v42
	v_exp_f32_e32 v5, v5
	v_sub_f32_e32 v6, v6, v42
	v_add_f32_e32 v60, 0, v59
	v_exp_f32_e32 v6, v6
	v_sub_f32_e32 v7, v7, v42
	v_add_f32_e32 v60, v3, v60
	v_exp_f32_e32 v7, v7
	v_add_f32_e32 v60, v4, v60
	v_add_f32_e32 v60, v5, v60
	v_sub_f32_e32 v8, v8, v42
	v_add_f32_e32 v60, v6, v60
	v_exp_f32_e32 v8, v8
	v_sub_f32_e32 v9, v9, v42
	v_sub_f32_e32 v10, v10, v42
	v_sub_f32_e32 v11, v11, v42
	v_exp_f32_e32 v9, v9
	v_exp_f32_e32 v61, v10
	v_add_f32_e32 v10, v7, v60
	v_exp_f32_e32 v60, v11
	v_sub_f32_e32 v11, v12, v42
	v_exp_f32_e32 v62, v11
	v_sub_f32_e32 v11, v13, v42
	v_exp_f32_e32 v63, v11
	v_sub_f32_e32 v11, v14, v42
	v_add_f32_e32 v10, v8, v10
	v_exp_f32_e32 v64, v11
	v_sub_f32_e32 v11, v15, v42
	v_add_f32_e32 v10, v9, v10
	v_exp_f32_e32 v65, v11
	v_sub_f32_e32 v11, v16, v42
	v_add_f32_e32 v10, v61, v10
	v_exp_f32_e32 v66, v11
	v_sub_f32_e32 v11, v17, v42
	v_add_f32_e32 v10, v60, v10
	v_exp_f32_e32 v67, v11
	v_sub_f32_e32 v11, v141, v42
	v_add_f32_e32 v10, v62, v10
	v_exp_f32_e32 v68, v11
	v_sub_f32_e32 v11, v142, v42
	v_add_f32_e32 v10, v63, v10
	v_exp_f32_e32 v69, v11
	v_sub_f32_e32 v11, v20, v42
	v_add_f32_e32 v10, v64, v10
	v_exp_f32_e32 v70, v11
	v_sub_f32_e32 v11, v21, v42
	v_add_f32_e32 v10, v65, v10
	v_exp_f32_e32 v71, v11
	v_sub_f32_e32 v11, v22, v42
	v_add_f32_e32 v10, v66, v10
	v_exp_f32_e32 v72, v11
	v_sub_f32_e32 v11, v23, v42
	v_add_f32_e32 v10, v67, v10
	v_exp_f32_e32 v73, v11
	v_sub_f32_e32 v11, v24, v42
	v_add_f32_e32 v10, v68, v10
	v_exp_f32_e32 v74, v11
	v_sub_f32_e32 v11, v25, v42
	v_add_f32_e32 v10, v69, v10
	v_exp_f32_e32 v75, v11
	v_sub_f32_e32 v11, v26, v42
	v_add_f32_e32 v10, v70, v10
	v_exp_f32_e32 v76, v11
	v_sub_f32_e32 v11, v27, v42
	v_add_f32_e32 v10, v71, v10
	v_exp_f32_e32 v77, v11
	v_sub_f32_e32 v11, v28, v42
	v_add_f32_e32 v10, v72, v10
	v_exp_f32_e32 v78, v11
	v_sub_f32_e32 v11, v29, v42
	v_add_f32_e32 v10, v73, v10
	v_exp_f32_e32 v79, v11
	v_sub_f32_e32 v11, v30, v42
	v_add_f32_e32 v10, v74, v10
	v_exp_f32_e32 v80, v11
	v_sub_f32_e32 v11, v31, v42
	v_add_f32_e32 v10, v75, v10
	v_exp_f32_e32 v81, v11
	v_sub_f32_e32 v11, v32, v42
	v_add_f32_e32 v10, v76, v10
	v_exp_f32_e32 v140, v11
	v_sub_f32_e32 v11, v33, v42
	v_add_f32_e32 v10, v77, v10
	v_exp_f32_e32 v141, v11
	v_sub_f32_e32 v11, v143, v42
	v_add_f32_e32 v10, v78, v10
	v_exp_f32_e32 v142, v11
	v_sub_f32_e32 v11, v144, v42
	v_add_f32_e32 v10, v79, v10
	v_exp_f32_e32 v143, v11
	v_sub_f32_e32 v11, v145, v42
	v_add_f32_e32 v10, v80, v10
	v_exp_f32_e32 v144, v11
	v_sub_f32_e32 v11, v146, v42
	v_add_f32_e32 v10, v81, v10
	v_exp_f32_e32 v145, v11
	v_sub_f32_e32 v11, v147, v42
	v_add_f32_e32 v10, v140, v10
	v_exp_f32_e32 v146, v11
	v_sub_f32_e32 v11, v148, v42
	v_add_f32_e32 v10, v141, v10
	v_exp_f32_e32 v147, v11
	v_sub_f32_e32 v11, v149, v42
	v_add_f32_e32 v10, v142, v10
	v_exp_f32_e32 v148, v11
	v_sub_f32_e32 v11, v150, v42
	v_add_f32_e32 v10, v143, v10
	v_exp_f32_e32 v149, v11
	v_sub_f32_e32 v11, v151, v42
	v_add_f32_e32 v10, v144, v10
	v_exp_f32_e32 v150, v11
	v_sub_f32_e32 v11, v152, v42
	v_add_f32_e32 v10, v145, v10
	v_exp_f32_e32 v151, v11
	v_sub_f32_e32 v11, v153, v42
	v_add_f32_e32 v10, v146, v10
	v_exp_f32_e32 v152, v11
	v_sub_f32_e32 v11, v155, v42
	v_add_f32_e32 v10, v147, v10
	v_exp_f32_e32 v153, v11
	v_sub_f32_e32 v11, v46, v42
	v_add_f32_e32 v10, v148, v10
	v_exp_f32_e32 v155, v11
	v_sub_f32_e32 v11, v156, v42
	v_add_f32_e32 v10, v149, v10
	v_exp_f32_e32 v156, v11
	v_sub_f32_e32 v11, v157, v42
	v_add_f32_e32 v10, v150, v10
	v_exp_f32_e32 v157, v11
	v_sub_f32_e32 v11, v158, v42
	v_add_f32_e32 v10, v151, v10
	v_exp_f32_e32 v158, v11
	v_sub_f32_e32 v11, v159, v42
	v_add_f32_e32 v10, v152, v10
	v_exp_f32_e32 v159, v11
	v_sub_f32_e32 v11, v160, v42
	v_add_f32_e32 v10, v153, v10
	v_exp_f32_e32 v160, v11
	v_sub_f32_e32 v11, v161, v42
	v_add_f32_e32 v10, v155, v10
	v_exp_f32_e32 v161, v11
	v_or_b32_e32 v11, s11, v95
	v_add_f32_e32 v10, v156, v10
	v_mad_u32_u24 v46, v11, s3, v97
	v_add_f32_e32 v10, v157, v10
	v_cvt_pk_bf16_f32 v20, v59, v3
	v_cvt_pk_bf16_f32 v21, v4, v5
	v_cvt_pk_bf16_f32 v22, v6, v7
	v_cvt_pk_bf16_f32 v23, v8, v9
	ds_read_b64_tr_b16 v[4:5], v46 offset:27648
	ds_read_b64_tr_b16 v[6:7], v46 offset:28800
	v_sub_f32_e32 v2, v2, v42
	v_add_f32_e32 v10, v158, v10
	v_exp_f32_e32 v162, v2
	v_add_f32_e32 v10, v159, v10
	v_add_f32_e32 v2, v160, v10
	v_add_f32_e32 v24, v161, v2
	s_waitcnt lgkmcnt(0)
	v_mfma_f32_32x32x16_bf16 v[2:17], v[20:23], v[4:7], 0
	v_add_f32_e32 v59, v162, v24
	ds_read_b64_tr_b16 v[24:25], v46 offset:27712
	ds_read_b64_tr_b16 v[26:27], v46 offset:28864
	v_cvt_pk_bf16_f32 v60, v61, v60
	v_cvt_pk_bf16_f32 v61, v62, v63
	v_cvt_pk_bf16_f32 v62, v64, v65
	v_cvt_pk_bf16_f32 v63, v66, v67
	ds_read_b64_tr_b16 v[64:65], v46 offset:29952
	ds_read_b64_tr_b16 v[66:67], v46 offset:31104
	v_sub_f32_e32 v19, v19, v42
	v_sub_f32_e32 v18, v18, v42
	v_exp_f32_e32 v163, v19
	v_exp_f32_e32 v164, v18
	s_waitcnt lgkmcnt(2)
	v_mfma_f32_32x32x16_bf16 v[18:33], v[20:23], v[24:27], 0
	v_sub_f32_e32 v139, v139, v42
	v_exp_f32_e32 v139, v139
	v_sub_f32_e32 v103, v103, v42
	v_exp_f32_e32 v103, v103
	v_sub_f32_e32 v101, v101, v42
	v_add_f32_e32 v59, v163, v59
	v_exp_f32_e32 v101, v101
	s_waitcnt lgkmcnt(0)
	v_mfma_f32_32x32x16_bf16 v[2:17], v[60:63], v[64:67], v[2:17]
	ds_read_b64_tr_b16 v[64:65], v46 offset:30016
	ds_read_b64_tr_b16 v[66:67], v46 offset:31168
	v_sub_f32_e32 v58, v58, v42
	v_add_f32_e32 v59, v164, v59
	v_add_f32_e32 v59, v139, v59
	v_sub_f32_e32 v57, v57, v42
	v_sub_f32_e32 v56, v56, v42
	v_sub_f32_e32 v55, v55, v42
	s_waitcnt lgkmcnt(0)
; #define LAS __attribute__((address_space(3)))
; __device__ __forceinline__ unsigned cvtpk(float lo, float hi) { f32x2 v = {lo, hi}; bf16x2_t b = __builtin_convertvector(v, bf16x2_t); return __builtin_bit_cast(unsigned, b); }
; __device__ __forceinline__ void swa_unit(Frame& F, int b, int kvh, int qb) {
;     ...
;         const int vrow0 = 32 * sub + 4 * hi + ((lane & 15) >> 2), vcol = ((lane >> 4) & 1) * 32 + (lane & 3) * 8;
; #pragma unroll
;         for (int j = 0; j < 5; ++j)
; #pragma unroll
;             for (int s = 0; s < 2; ++s) {
;                 u32x4 pw; pw.x = cvtpk(p[j][8 * s], p[j][8 * s + 1]); pw.y = cvtpk(p[j][8 * s + 2], p[j][8 * s + 3]); pw.z = cvtpk(p[j][8 * s + 4], p[j][8 * s + 5]); pw.w = cvtpk(p[j][8 * s + 6], p[j][8 * s + 7]);
;                 const bf16x8 pa = __builtin_bit_cast(bf16x8, pw);
; #pragma unroll
;                 for (int d0 = 0; d0 < 2; ++d0) { const LAS unsigned char* vp = Vl + (vrow0 + 32 * j + 16 * s) * SWA_KROW + d0 * 64 + vcol;
;                     const s16x4 lo = __builtin_bit_cast(s16x4, __builtin_amdgcn_ds_read_tr16_b64_v4i16((LAS s16x4*)vp));
;                     const s16x4 hh = __builtin_bit_cast(s16x4, __builtin_amdgcn_ds_read_tr16_b64_v4i16((LAS s16x4*)(vp + 8 * SWA_KROW)));
;                     const bf16x8 vf = (bf16x8){lo[0], lo[1], lo[2], lo[3], hh[0], hh[1], hh[2], hh[3]};
;                     o[d0] = __builtin_amdgcn_mfma_f32_32x32x16_bf16(pa, vf, o[d0], 0, 0, 0); } }
;         if (hi == 0) wsf[r32] = 1.0f / sum;
	v_mfma_f32_32x32x16_bf16 v[18:33], v[60:63], v[64:67], v[18:33]
	v_cvt_pk_bf16_f32 v60, v68, v69
	v_cvt_pk_bf16_f32 v61, v70, v71
	v_cvt_pk_bf16_f32 v62, v72, v73
	v_cvt_pk_bf16_f32 v63, v74, v75
	ds_read_b64_tr_b16 v[64:65], v46 offset:32256
	ds_read_b64_tr_b16 v[66:67], v46 offset:33408
	v_exp_f32_e32 v68, v58
	v_add_f32_e32 v58, v103, v59
	s_waitcnt lgkmcnt(0)
	v_mfma_f32_32x32x16_bf16 v[2:17], v[60:63], v[64:67], v[2:17]
	ds_read_b64_tr_b16 v[64:65], v46 offset:32320
	ds_read_b64_tr_b16 v[66:67], v46 offset:33472
	v_add_f32_e32 v58, v101, v58
	v_add_f32_e32 v69, v68, v58
	v_exp_f32_e32 v70, v57
	v_exp_f32_e32 v71, v56
	v_cvt_pk_bf16_f32 v56, v76, v77
	v_cvt_pk_bf16_f32 v57, v78, v79
	s_waitcnt lgkmcnt(0)
	v_mfma_f32_32x32x16_bf16 v[18:33], v[60:63], v[64:67], v[18:33]
	v_cvt_pk_bf16_f32 v58, v80, v81
	v_cvt_pk_bf16_f32 v59, v140, v141
	ds_read_b64_tr_b16 v[60:61], v46 offset:34560
	ds_read_b64_tr_b16 v[62:63], v46 offset:35712
	v_exp_f32_e32 v64, v55
	v_add_f32_e32 v55, v70, v69
	v_add_f32_e32 v55, v71, v55
	v_sub_f32_e32 v54, v54, v42
	s_waitcnt lgkmcnt(0)
	v_mfma_f32_32x32x16_bf16 v[2:17], v[56:59], v[60:63], v[2:17]
	ds_read_b64_tr_b16 v[60:61], v46 offset:34624
	ds_read_b64_tr_b16 v[62:63], v46 offset:35776
	v_add_f32_e32 v65, v64, v55
	v_exp_f32_e32 v66, v54
	v_cvt_pk_bf16_f32 v54, v142, v143
	v_cvt_pk_bf16_f32 v55, v144, v145
	v_sub_f32_e32 v53, v53, v42
	v_exp_f32_e32 v67, v53
	s_waitcnt lgkmcnt(0)
	v_mfma_f32_32x32x16_bf16 v[18:33], v[56:59], v[60:63], v[18:33]
	v_cvt_pk_bf16_f32 v56, v146, v147
	v_cvt_pk_bf16_f32 v57, v148, v149
	ds_read_b64_tr_b16 v[58:59], v46 offset:36864
	ds_read_b64_tr_b16 v[60:61], v46 offset:38016
	v_sub_f32_e32 v52, v52, v42
	v_exp_f32_e32 v62, v52
	v_add_f32_e32 v52, v66, v65
	v_add_f32_e32 v52, v67, v52
	s_waitcnt lgkmcnt(0)
	v_mfma_f32_32x32x16_bf16 v[2:17], v[54:57], v[58:61], v[2:17]
	ds_read_b64_tr_b16 v[58:59], v46 offset:36928
	ds_read_b64_tr_b16 v[60:61], v46 offset:38080
	v_sub_f32_e32 v51, v51, v42
	v_sub_f32_e32 v50, v50, v42
	v_add_f32_e32 v63, v62, v52
	v_exp_f32_e32 v65, v51
	v_exp_f32_e32 v69, v50
	v_cvt_pk_bf16_f32 v50, v150, v151
	s_waitcnt lgkmcnt(0)
	v_mfma_f32_32x32x16_bf16 v[18:33], v[54:57], v[58:61], v[18:33]
	v_cvt_pk_bf16_f32 v51, v152, v153
	v_cvt_pk_bf16_f32 v52, v155, v156
	v_cvt_pk_bf16_f32 v53, v157, v158
	ds_read_b64_tr_b16 v[54:55], v46 offset:39168
	ds_read_b64_tr_b16 v[56:57], v46 offset:40320
	v_sub_f32_e32 v49, v49, v42
	v_exp_f32_e32 v58, v49
	v_add_f32_e32 v49, v65, v63
	s_waitcnt lgkmcnt(0)
	v_mfma_f32_32x32x16_bf16 v[2:17], v[50:53], v[54:57], v[2:17]
	ds_read_b64_tr_b16 v[54:55], v46 offset:39232
	ds_read_b64_tr_b16 v[56:57], v46 offset:40384
	v_add_f32_e32 v49, v69, v49
	v_sub_f32_e32 v48, v48, v42
	v_add_f32_e32 v59, v58, v49
	v_exp_f32_e32 v60, v48
	v_cvt_pk_bf16_f32 v48, v159, v160
	v_cvt_pk_bf16_f32 v49, v161, v162
	s_waitcnt lgkmcnt(0)
	v_mfma_f32_32x32x16_bf16 v[18:33], v[50:53], v[54:57], v[18:33]
	v_cvt_pk_bf16_f32 v50, v163, v164
	v_cvt_pk_bf16_f32 v51, v139, v103
	ds_read_b64_tr_b16 v[52:53], v46 offset:41472
	ds_read_b64_tr_b16 v[54:55], v46 offset:42624
	v_sub_f32_e32 v47, v47, v42
	v_sub_f32_e32 v45, v45, v42
	v_sub_f32_e32 v44, v44, v42
	v_sub_f32_e32 v43, v43, v42
	s_waitcnt lgkmcnt(0)
	v_mfma_f32_32x32x16_bf16 v[2:17], v[48:51], v[52:55], v[2:17]
	ds_read_b64_tr_b16 v[52:53], v46 offset:41536
	ds_read_b64_tr_b16 v[54:55], v46 offset:42688
	v_exp_f32_e32 v61, v47
	v_exp_f32_e32 v45, v45
	v_exp_f32_e32 v44, v44
	v_exp_f32_e32 v43, v43
	v_sub_f32_e32 v41, v41, v42
	v_sub_f32_e32 v40, v40, v42
	s_waitcnt lgkmcnt(0)
	v_mfma_f32_32x32x16_bf16 v[18:33], v[48:51], v[52:55], v[18:33]
	v_cvt_pk_bf16_f32 v48, v101, v68
	v_cvt_pk_bf16_f32 v49, v70, v71
	v_cvt_pk_bf16_f32 v50, v64, v66
	v_cvt_pk_bf16_f32 v51, v67, v62
	ds_read_b64_tr_b16 v[52:53], v46 offset:43776
	ds_read_b64_tr_b16 v[54:55], v46 offset:44928
	v_sub_f32_e32 v39, v39, v42
	v_add_f32_e32 v47, v60, v59
	s_waitcnt lgkmcnt(0)
	v_mfma_f32_32x32x16_bf16 v[2:17], v[48:51], v[52:55], v[2:17]
	ds_read_b64_tr_b16 v[52:53], v46 offset:43840
	ds_read_b64_tr_b16 v[54:55], v46 offset:44992
	v_exp_f32_e32 v56, v41
	v_exp_f32_e32 v57, v40
	v_exp_f32_e32 v59, v39
	v_sub_f32_e32 v62, v38, v42
	v_cvt_pk_bf16_f32 v38, v65, v69
	v_cvt_pk_bf16_f32 v39, v58, v60
	s_waitcnt lgkmcnt(0)
	v_mfma_f32_32x32x16_bf16 v[18:33], v[48:51], v[52:55], v[18:33]
	v_cvt_pk_bf16_f32 v40, v61, v45
	v_cvt_pk_bf16_f32 v41, v44, v43
	ds_read_b64_tr_b16 v[48:49], v46 offset:46080
	ds_read_b64_tr_b16 v[50:51], v46 offset:47232
	v_add_f32_e32 v47, v61, v47
	v_add_f32_e32 v47, v45, v47
	v_add_f32_e32 v47, v44, v47
	v_sub_f32_e32 v37, v37, v42
	v_sub_f32_e32 v36, v36, v42
	s_waitcnt lgkmcnt(0)
	v_mfma_f32_32x32x16_bf16 v[2:17], v[38:41], v[48:51], v[2:17]
	ds_read_b64_tr_b16 v[48:49], v46 offset:46144
	ds_read_b64_tr_b16 v[50:51], v46 offset:47296
	v_sub_f32_e32 v35, v35, v42
	v_sub_f32_e32 v34, v34, v42
	v_add_f32_e32 v47, v43, v47
	v_exp_f32_e32 v52, v62
	v_exp_f32_e32 v53, v37
	v_exp_f32_e32 v43, v36
	v_exp_f32_e32 v44, v35
	v_exp_f32_e32 v45, v34
	s_waitcnt lgkmcnt(0)
	v_mfma_f32_32x32x16_bf16 v[18:33], v[38:41], v[48:51], v[18:33]
	v_cvt_pk_bf16_f32 v34, v56, v57
	v_cvt_pk_bf16_f32 v35, v59, v52
	v_cvt_pk_bf16_f32 v36, v53, v43
	v_cvt_pk_bf16_f32 v37, v44, v45
	ds_read_b64_tr_b16 v[38:39], v46 offset:48384
	ds_read_b64_tr_b16 v[40:41], v46 offset:49536
	v_add_f32_e32 v47, v56, v47
	v_add_f32_e32 v47, v57, v47
	s_waitcnt lgkmcnt(0)
	v_mfma_f32_32x32x16_bf16 v[2:17], v[34:37], v[38:41], v[2:17]
	ds_read_b64_tr_b16 v[38:39], v46 offset:48448
	ds_read_b64_tr_b16 v[40:41], v46 offset:49600
	v_add_f32_e32 v47, v59, v47
	v_add_f32_e32 v47, v52, v47
	v_add_f32_e32 v47, v53, v47
	v_add_f32_e32 v43, v43, v47
	v_add_f32_e32 v43, v44, v43
	v_add_f32_e32 v43, v45, v43
	s_waitcnt lgkmcnt(0)
	v_mfma_f32_32x32x16_bf16 v[18:33], v[34:37], v[38:41], v[18:33]
	ds_bpermute_b32 v44, v110, v43
	s_and_saveexec_b64 s[86:87], s[6:7]
	s_cbranch_execz .LBB0_283
	v_sub_f32_e32 v34, v99, v42
	v_exp_f32_e32 v34, v34
	s_waitcnt lgkmcnt(0)
	v_add_f32_e32 v35, v43, v44
	v_add_f32_e32 v34, v34, v35
	v_div_scale_f32 v35, vcc, v34, v34, 1.0
	v_rcp_f32_e32 v36, v35
	v_div_scale_f32 v37, vcc, 1.0, v34, 1.0
	v_fma_f32 v38, -v35, v36, 1.0
	v_fmac_f32_e32 v36, v38, v36
	v_mul_f32_e32 v38, v37, v36
	v_fma_f32 v39, -v35, v38, v37
	v_fmac_f32_e32 v38, v39, v36
	v_fma_f32 v35, -v35, v38, v37
	v_div_fmas_f32 v35, v35, v36, v38
	v_div_fixup_f32 v34, v35, v34, 1.0
	ds_write_b32 v104, v34 offset:55296
	s_branch .LBB0_283
